# attn_k work rebalanced: older waves 0-3 process 5 query tiles, younger waves 4-7 process 3 (younger half is the VALU arbitration loser)
# speedup vs baseline: 1.0195x; 1.0033x over previous
_Z6attn_kPKDF16_S0_S0_PDF16_:
	v_readfirstlane_b32 s13, v0
	s_movk_i32 s14, 0x200
	s_nop 2
	s_cmpk_lt_u32 s13, 0x100
	s_cselect_b32 s14, 0x380, s14
	s_add_i32 s15, s14, 0x100
	s_load_dwordx8 s[4:11], s[0:1], 0x0
	s_lshr_b32 s1, s2, 2
	s_and_b32 s0, s2, 7
	s_and_b32 s1, s1, 8
	s_or_b32 s0, s1, s0
	s_lshr_b32 s3, s2, 6
	s_lshl_b32 s1, s3, 8
	s_lshl_b32 s12, s0, 6
	s_lshl_b32 s0, s0, 7
	s_waitcnt lgkmcnt(0)
	s_add_u32 s6, s6, s0
	v_lshlrev_b32_e32 v1, 4, v0
	s_addc_u32 s7, s7, 0
	v_and_b32_e32 v180, 0x70, v1
	v_mov_b32_e32 v181, 0
	v_lshrrev_b32_e32 v36, 3, v0
	v_or_b32_e32 v22, 0x200, v0
	v_lshl_add_u64 v[10:11], s[6:7], 0, v[180:181]
	v_or_b32_e32 v180, s1, v36
	v_lshrrev_b32_e32 v37, 3, v22
	v_or_b32_e32 v32, 0x400, v0
	v_lshlrev_b64 v[2:3], 11, v[180:181]
	v_or_b32_e32 v180, s1, v37
	v_lshrrev_b32_e32 v38, 3, v32
	v_or_b32_e32 v33, 0x600, v0
	v_lshl_add_u64 v[12:13], v[10:11], 0, v[2:3]
	v_lshlrev_b64 v[2:3], 11, v[180:181]
	v_or_b32_e32 v180, s1, v38
	v_lshrrev_b32_e32 v39, 3, v33
	v_lshl_add_u64 v[14:15], v[10:11], 0, v[2:3]
	global_load_dwordx4 v[2:5], v[12:13], off
	global_load_dwordx4 v[6:9], v[14:15], off
	v_lshlrev_b64 v[12:13], 11, v[180:181]
	v_or_b32_e32 v180, s1, v39
	v_and_b32_e32 v40, 31, v0
	s_lshl_b32 s1, s3, 10
	v_lshl_add_u64 v[18:19], v[10:11], 0, v[12:13]
	v_lshlrev_b64 v[12:13], 11, v[180:181]
	s_or_b32 s1, s12, s1
	v_lshlrev_b32_e32 v180, 4, v40
	v_lshrrev_b32_e32 v41, 5, v0
	v_lshl_add_u64 v[20:21], v[10:11], 0, v[12:13]
	global_load_dwordx4 v[10:13], v[18:19], off
	global_load_dwordx4 v[14:17], v[20:21], off
	v_lshl_add_u64 v[30:31], s[8:9], 0, v[180:181]
	v_or_b32_e32 v180, s1, v41
	v_lshrrev_b32_e32 v42, 5, v22
	v_lshlrev_b64 v[18:19], 9, v[180:181]
	v_or_b32_e32 v180, s1, v42
	v_lshrrev_b32_e32 v43, 5, v32
	v_lshl_add_u64 v[26:27], v[30:31], 0, v[18:19]
	v_lshlrev_b64 v[18:19], 9, v[180:181]
	v_or_b32_e32 v180, s1, v43
	v_lshl_add_u64 v[28:29], v[30:31], 0, v[18:19]
	global_load_dwordx4 v[18:21], v[26:27], off
	global_load_dwordx4 v[22:25], v[28:29], off
	v_lshlrev_b64 v[26:27], 9, v[180:181]
	v_lshl_add_u64 v[26:27], v[30:31], 0, v[26:27]
	global_load_dwordx4 v[26:29], v[26:27], off
	v_lshrrev_b32_e32 v45, 6, v0
	s_lshl_b32 s2, s2, 7
	v_lshrrev_b32_e32 v44, 5, v33
	s_and_b32 s6, s2, 0xc00
	v_lshlrev_b32_e32 v47, 5, v45
	v_or_b32_e32 v180, s1, v44
	v_or_b32_e32 v34, s6, v47
	s_lshl_b32 s7, s3, 12
	v_lshlrev_b64 v[32:33], 9, v[180:181]
	v_or3_b32 v180, s7, v40, v34
	v_lshlrev_b64 v[34:35], 11, v[180:181]
	v_bfe_u32 v46, v0, 5, 1
	s_mov_b32 s1, 0
	v_lshl_add_u64 v[34:35], s[4:5], 0, v[34:35]
	v_lshl_add_u64 v[34:35], v[34:35], 0, s[0:1]
	v_lshlrev_b32_e32 v180, 4, v46
	v_lshl_add_u64 v[30:31], v[30:31], 0, v[32:33]
	v_lshl_add_u64 v[34:35], v[34:35], 0, v[180:181]
	global_load_dwordx4 v[30:33], v[30:31], off
	s_nop 0
	global_load_dwordx4 v[120:123], v[34:35], off
	global_load_dwordx4 v[124:127], v[34:35], off offset:32
	global_load_dwordx4 v[116:119], v[34:35], off offset:64
	global_load_dwordx4 v[112:115], v[34:35], off offset:96
	s_movk_i32 s2, 0x70
	v_bitop3_b32 v1, v1, s2, v0 bitop3:0x48
	v_lshl_or_b32 v35, v36, 7, v1
	v_lshl_or_b32 v36, v37, 7, v1
	v_lshl_or_b32 v37, v38, 7, v1
	v_lshl_or_b32 v1, v39, 7, v1
	s_add_u32 s2, s4, s0
	v_mul_u32_u24_e32 v34, 0x1200, v45
	s_addc_u32 s3, s5, 0
	v_lshl_add_u64 v[182:183], s[2:3], 0, v[180:181]
	s_movk_i32 s2, 0x90
	s_waitcnt vmcnt(11)
	ds_write_b128 v35, v[2:5]
	s_waitcnt vmcnt(10)
	ds_write_b128 v36, v[6:9]
	s_waitcnt vmcnt(9)
	ds_write_b128 v37, v[10:13]
	s_waitcnt vmcnt(8)
	ds_write_b128 v1, v[14:17]
	v_bitop3_b32 v1, v41, v0, 31 bitop3:0x78
	v_lshlrev_b32_e32 v1, 4, v1
	v_lshl_or_b32 v2, v41, 9, v1
	v_lshlrev_b32_e32 v3, 1, v0
	v_lshrrev_b32_e32 v4, 1, v0
	v_and_b32_e32 v3, 8, v3
	v_and_b32_e32 v4, 4, v4
	s_waitcnt vmcnt(7)
	ds_write_b128 v2, v[18:21] offset:32768
	v_lshl_or_b32 v2, v42, 9, v1
	s_waitcnt vmcnt(6)
	ds_write_b128 v2, v[22:25] offset:32768
	v_lshl_or_b32 v2, v43, 9, v1
	s_waitcnt vmcnt(5)
	ds_write_b128 v2, v[26:29] offset:32768
	v_and_b32_e32 v2, 19, v0
	v_or3_b32 v2, v3, v2, v4
	v_lshrrev_b32_e32 v4, 1, v2
	v_lshlrev_b32_e32 v3, 7, v2
	v_bfe_u32 v2, v2, 1, 3
	v_bitop3_b32 v4, v46, v4, 7 bitop3:0x78
	v_lshl_or_b32 v186, v4, 4, v3
	v_bitop3_b32 v4, v46, v2, 2 bitop3:0x36
	v_lshl_or_b32 v187, v4, 4, v3
	v_bitop3_b32 v4, v46, v2, 4 bitop3:0x36
	v_bitop3_b32 v2, v46, v2, 6 bitop3:0x36
	v_lshl_or_b32 v188, v4, 4, v3
	v_lshl_or_b32 v189, v2, 4, v3
	v_lshlrev_b32_e32 v2, 9, v40
	v_and_b32_e32 v3, 15, v0
	v_bitop3_b32 v4, v46, v0, 15 bitop3:0x78
	v_lshl_or_b32 v190, v4, 4, v2
	v_bitop3_b32 v4, v46, v3, 2 bitop3:0x36
	v_lshl_or_b32 v191, v4, 4, v2
	v_bitop3_b32 v4, v46, v3, 4 bitop3:0x36
	v_lshl_or_b32 v192, v4, 4, v2
	v_bitop3_b32 v4, v46, v3, 6 bitop3:0x36
	v_lshl_or_b32 v193, v4, 4, v2
	v_bitop3_b32 v4, v46, v3, 8 bitop3:0x36
	v_lshl_or_b32 v194, v4, 4, v2
	v_bitop3_b32 v4, v46, v3, 10 bitop3:0x36
	v_lshl_or_b32 v195, v4, 4, v2
	v_bitop3_b32 v4, v46, v3, 12 bitop3:0x36
	v_bitop3_b32 v3, v46, v3, 14 bitop3:0x36
	v_lshl_or_b32 v197, v3, 4, v2
	v_mbcnt_lo_u32_b32 v3, -1, 0
	v_mbcnt_hi_u32_b32 v3, -1, v3
	v_and_b32_e32 v5, 64, v3
	v_lshl_or_b32 v196, v4, 4, v2
	v_xor_b32_e32 v4, 32, v3
	v_add_u32_e32 v5, 64, v5
	v_cmp_lt_i32_e32 vcc, v4, v5
	v_or_b32_e32 v2, 0x10000, v34
	v_lshl_or_b32 v1, v44, 9, v1
	v_cndmask_b32_e32 v3, v3, v4, vcc
	v_lshlrev_b32_e32 v198, 2, v3
	v_mad_u32_u24 v3, v40, s2, v2
	v_bfe_u32 v4, v0, 3, 3
	v_and_b32_e32 v0, 7, v0
	s_add_u32 s2, s10, s0
	v_lshlrev_b32_e32 v180, 4, v0
	s_addc_u32 s3, s11, 0
	v_or_b32_e32 v5, 8, v4
	s_or_b32 s0, s7, s6
	s_waitcnt vmcnt(4)
	ds_write_b128 v1, v[30:33] offset:32768
	v_lshlrev_b32_e32 v1, 3, v46
	s_waitcnt lgkmcnt(0)
	s_barrier
	s_waitcnt vmcnt(3)
	s_waitcnt vmcnt(2)
	s_waitcnt vmcnt(1)
	s_waitcnt vmcnt(0)
	v_or_b32_e32 v0, v2, v180
	v_mul_u32_u24_e32 v2, 0x90, v4
	v_mul_u32_u24_e32 v5, 0x90, v5
	v_or_b32_e32 v6, s0, v47
	s_movk_i32 s0, 0x100
	v_mov_b64_e32 v[96:97], v[120:121]
	v_mov_b64_e32 v[100:101], v[124:125]
	v_mov_b64_e32 v[104:105], v[116:117]
	v_mov_b64_e32 v[108:109], v[112:113]
	v_lshl_add_u64 v[184:185], s[2:3], 0, v[180:181]
	v_or3_b32 v199, v6, v40, s0
	v_or_b32_e32 v200, v6, v4
	s_mov_b32 s0, 0xf149f2ca
	v_add_u32_e32 v201, v3, v1
	v_add_u32_e32 v202, v0, v2
	v_add_u32_e32 v203, v0, v5
	v_mov_b64_e32 v[98:99], v[122:123]
	v_mov_b64_e32 v[102:103], v[126:127]
	v_mov_b64_e32 v[106:107], v[118:119]
	v_mov_b64_e32 v[110:111], v[114:115]
	s_branch .LBB5_2
.LBB5_1:
	ds_read_b128 v[0:3], v186
	ds_read_b128 v[4:7], v186 offset:4096
	ds_read_b128 v[8:11], v187
	ds_read_b128 v[12:15], v187 offset:4096
	ds_read_b128 v[16:19], v188
	ds_read_b128 v[20:23], v188 offset:4096
	ds_read_b128 v[24:27], v189
	ds_read_b128 v[28:31], v189 offset:4096
	ds_read_b128 v[64:67], v186 offset:8192
	ds_read_b128 v[68:71], v186 offset:12288
	ds_read_b128 v[72:75], v187 offset:8192
	ds_read_b128 v[76:79], v187 offset:12288
	ds_read_b128 v[80:83], v188 offset:8192
	ds_read_b128 v[84:87], v188 offset:12288
	ds_read_b128 v[88:91], v189 offset:8192
	ds_read_b128 v[160:163], v189 offset:12288
	s_waitcnt lgkmcnt(14)
	v_mfma_f32_32x32x16_f16 v[48:63], v[0:3], v[120:123], 0
	ds_read_b128 v[152:155], v190 offset:32768
	ds_read_b128 v[156:159], v190 offset:49152
	ds_read_b128 v[148:151], v191 offset:32768
	ds_read_b128 v[144:147], v191 offset:49152
	ds_read_b128 v[140:143], v192 offset:32768
	ds_read_b128 v[136:139], v192 offset:49152
	ds_read_b128 v[132:135], v193 offset:32768
	ds_read_b128 v[92:95], v193 offset:49152
	v_mfma_f32_32x32x16_f16 v[32:47], v[4:7], v[120:123], 0
	s_waitcnt lgkmcnt(14)
	v_mfma_f32_32x32x16_f16 v[48:63], v[8:11], v[124:127], v[48:63]
	v_mfma_f32_32x32x16_f16 v[32:47], v[12:15], v[124:127], v[32:47]
	v_mfma_f32_32x32x16_f16 v[48:63], v[16:19], v[116:119], v[48:63]
	v_mfma_f32_32x32x16_f16 v[32:47], v[20:23], v[116:119], v[32:47]
	v_mfma_f32_32x32x16_f16 v[48:63], v[24:27], v[112:115], v[48:63]
	v_mfma_f32_32x32x16_f16 v[32:47], v[28:31], v[112:115], v[32:47]
	v_mfma_f32_32x32x16_f16 v[16:31], v[64:67], v[120:123], 0
	s_waitcnt lgkmcnt(13)
	v_mfma_f32_32x32x16_f16 v[16:31], v[72:75], v[124:127], v[16:31]
	v_mfma_f32_32x32x16_f16 v[0:15], v[68:71], v[120:123], 0
	s_waitcnt lgkmcnt(11)
	v_mfma_f32_32x32x16_f16 v[16:31], v[80:83], v[116:119], v[16:31]
	v_mfma_f32_32x32x16_f16 v[0:15], v[76:79], v[124:127], v[0:15]
	s_waitcnt lgkmcnt(9)
	v_mfma_f32_32x32x16_f16 v[16:31], v[88:91], v[112:115], v[16:31]
	v_mfma_f32_32x32x16_f16 v[0:15], v[84:87], v[116:119], v[0:15]
	ds_read_b128 v[128:131], v194 offset:32768
	ds_read_b128 v[88:91], v194 offset:49152
	ds_read_b128 v[84:87], v195 offset:32768
	ds_read_b128 v[80:83], v195 offset:49152
	ds_read_b128 v[76:79], v196 offset:32768
	ds_read_b128 v[72:75], v196 offset:49152
	ds_read_b128 v[68:71], v197 offset:32768
	ds_read_b128 v[64:67], v197 offset:49152
	s_waitcnt lgkmcnt(14)
	v_mfma_f32_32x32x16_f16 v[0:15], v[160:163], v[112:115], v[0:15]
	v_max_f32_e32 v160, v49, v49
	v_max_f32_e32 v161, v48, v48
	s_nop 9
	v_max_f32_e32 v163, v1, v1
	v_max_f32_e32 v164, v0, v0
	v_max_f32_e32 v160, v161, v160
	v_max_f32_e32 v161, v33, v33
	v_max_f32_e32 v162, v32, v32
	v_max_f32_e32 v163, v164, v163
	v_max_f32_e32 v161, v162, v161
	v_max3_f32 v162, v16, v17, v18
	v_max3_f32 v163, v163, v2, v3
	v_max3_f32 v160, v160, v50, v51
	v_max3_f32 v161, v161, v34, v35
	v_max3_f32 v162, v162, v19, v20
	v_max3_f32 v163, v163, v4, v5
	v_max3_f32 v160, v160, v52, v53
	v_max3_f32 v161, v161, v36, v37
	v_max3_f32 v162, v162, v21, v22
	v_max3_f32 v163, v163, v6, v7
	v_max3_f32 v160, v160, v54, v55
	v_max3_f32 v161, v161, v38, v39
	v_max3_f32 v162, v162, v23, v24
	v_max3_f32 v163, v163, v8, v9
	v_max3_f32 v160, v160, v56, v57
	v_max3_f32 v161, v161, v40, v41
	v_max3_f32 v162, v162, v25, v26
	v_max3_f32 v163, v163, v10, v11
	v_max3_f32 v160, v160, v58, v59
	v_max3_f32 v161, v161, v42, v43
	v_max3_f32 v162, v162, v27, v28
	v_max3_f32 v163, v163, v12, v13
	v_max3_f32 v160, v160, v60, v61
	v_max3_f32 v161, v161, v44, v45
	v_max3_f32 v162, v162, v29, v30
	v_max3_f32 v163, v163, v14, v15
	v_max3_f32 v160, v160, v62, v63
	v_max3_f32 v161, v161, v46, v47
	v_max3_f32 v162, v162, v31, v163
	v_max3_f32 v160, v160, v161, v162
	ds_bpermute_b32 v161, v198, v160
	s_waitcnt lgkmcnt(0)
	v_max3_f32 v180, v160, v161, s0
	v_sub_f32_e32 v48, v48, v180
	v_sub_f32_e32 v32, v32, v180
	v_exp_f32_e32 v48, v48
	v_sub_f32_e32 v49, v49, v180
	v_exp_f32_e32 v162, v32
	v_sub_f32_e32 v32, v33, v180
	v_exp_f32_e32 v49, v49
	v_sub_f32_e32 v50, v50, v180
	v_exp_f32_e32 v163, v32
	v_sub_f32_e32 v32, v34, v180
	v_exp_f32_e32 v50, v50
	v_sub_f32_e32 v51, v51, v180
	v_exp_f32_e32 v164, v32
	v_sub_f32_e32 v32, v35, v180
	v_exp_f32_e32 v51, v51
	v_sub_f32_e32 v52, v52, v180
	v_exp_f32_e32 v165, v32
	v_sub_f32_e32 v33, v36, v180
	v_add_f32_e32 v161, 0, v48
	v_exp_f32_e32 v52, v52
	v_sub_f32_e32 v53, v53, v180
	v_add_f32_e32 v32, 0, v162
	v_exp_f32_e32 v36, v33
	v_sub_f32_e32 v33, v37, v180
	v_add_f32_e32 v161, v161, v49
	v_exp_f32_e32 v53, v53
	v_sub_f32_e32 v54, v54, v180
	v_add_f32_e32 v32, v32, v163
	v_exp_f32_e32 v37, v33
	v_sub_f32_e32 v33, v38, v180
	v_add_f32_e32 v161, v161, v50
	v_exp_f32_e32 v54, v54
	v_sub_f32_e32 v55, v55, v180
	v_add_f32_e32 v32, v32, v164
	v_exp_f32_e32 v38, v33
	v_sub_f32_e32 v33, v39, v180
	v_add_f32_e32 v161, v161, v51
	v_exp_f32_e32 v55, v55
	v_sub_f32_e32 v56, v56, v180
	v_add_f32_e32 v32, v32, v165
	v_exp_f32_e32 v39, v33
	v_sub_f32_e32 v33, v40, v180
	v_add_f32_e32 v161, v161, v52
	v_exp_f32_e32 v56, v56
	v_sub_f32_e32 v57, v57, v180
	v_add_f32_e32 v32, v32, v36
	v_exp_f32_e32 v40, v33
	v_sub_f32_e32 v33, v41, v180
	v_add_f32_e32 v161, v161, v53
	v_exp_f32_e32 v57, v57
	v_sub_f32_e32 v58, v58, v180
	v_add_f32_e32 v32, v32, v37
	v_exp_f32_e32 v166, v33
	v_sub_f32_e32 v33, v42, v180
	v_add_f32_e32 v161, v161, v54
	v_exp_f32_e32 v58, v58
	v_sub_f32_e32 v59, v59, v180
	v_add_f32_e32 v32, v32, v38
	v_exp_f32_e32 v41, v33
	v_sub_f32_e32 v33, v43, v180
	v_add_f32_e32 v161, v161, v55
	v_exp_f32_e32 v59, v59
	v_sub_f32_e32 v60, v60, v180
	v_add_f32_e32 v32, v32, v39
	v_exp_f32_e32 v167, v33
	v_sub_f32_e32 v33, v44, v180
	v_add_f32_e32 v161, v161, v56
	v_exp_f32_e32 v60, v60
	v_sub_f32_e32 v61, v61, v180
	v_add_f32_e32 v32, v32, v40
	v_exp_f32_e32 v42, v33
	v_sub_f32_e32 v33, v45, v180
	v_add_f32_e32 v161, v161, v57
	v_exp_f32_e32 v61, v61
	v_sub_f32_e32 v62, v62, v180
	v_add_f32_e32 v32, v32, v166
	v_exp_f32_e32 v44, v33
	v_sub_f32_e32 v33, v46, v180
	v_add_f32_e32 v161, v161, v58
	v_exp_f32_e32 v62, v62
	v_sub_f32_e32 v63, v63, v180
	v_add_f32_e32 v32, v32, v41
	v_exp_f32_e32 v43, v33
	v_sub_f32_e32 v33, v47, v180
	v_add_f32_e32 v161, v161, v59
	v_exp_f32_e32 v63, v63
	v_add_f32_e32 v32, v32, v167
	v_exp_f32_e32 v45, v33
	v_add_f32_e32 v161, v161, v60
	v_add_f32_e32 v32, v32, v42
	v_add_f32_e32 v161, v161, v61
	v_add_f32_e32 v32, v32, v44
	v_add_f32_e32 v161, v161, v62
	v_add_f32_e32 v32, v32, v43
	v_add_f32_e32 v161, v161, v63
	v_add_f32_e32 v32, v32, v45
	v_sub_f32_e32 v16, v16, v180
	v_sub_f32_e32 v0, v0, v180
	v_add_f32_e32 v32, v161, v32
	v_exp_f32_e32 v16, v16
	v_sub_f32_e32 v17, v17, v180
	v_exp_f32_e32 v161, v0
	v_sub_f32_e32 v0, v1, v180
	v_exp_f32_e32 v17, v17
	v_sub_f32_e32 v18, v18, v180
	v_exp_f32_e32 v168, v0
	v_sub_f32_e32 v0, v2, v180
	v_exp_f32_e32 v18, v18
	v_sub_f32_e32 v19, v19, v180
	v_exp_f32_e32 v169, v0
	v_sub_f32_e32 v0, v3, v180
	v_exp_f32_e32 v19, v19
	v_sub_f32_e32 v20, v20, v180
	v_exp_f32_e32 v170, v0
	v_sub_f32_e32 v1, v4, v180
	v_add_f32_e32 v33, 0, v16
	v_exp_f32_e32 v20, v20
	v_sub_f32_e32 v21, v21, v180
	v_add_f32_e32 v0, 0, v161
	v_exp_f32_e32 v4, v1
	v_sub_f32_e32 v1, v5, v180
	v_add_f32_e32 v33, v33, v17
	v_exp_f32_e32 v21, v21
	v_sub_f32_e32 v22, v22, v180
	v_add_f32_e32 v0, v0, v168
	v_exp_f32_e32 v5, v1
	v_sub_f32_e32 v1, v6, v180
	v_add_f32_e32 v33, v33, v18
	v_exp_f32_e32 v22, v22
	v_sub_f32_e32 v23, v23, v180
	v_add_f32_e32 v0, v0, v169
	v_exp_f32_e32 v6, v1
	v_sub_f32_e32 v1, v7, v180
	v_add_f32_e32 v33, v33, v19
	v_exp_f32_e32 v23, v23
	v_sub_f32_e32 v24, v24, v180
	v_add_f32_e32 v0, v0, v170
	v_exp_f32_e32 v7, v1
	v_sub_f32_e32 v1, v8, v180
	v_add_f32_e32 v33, v33, v20
	v_exp_f32_e32 v24, v24
	v_sub_f32_e32 v25, v25, v180
	v_add_f32_e32 v0, v0, v4
	v_exp_f32_e32 v8, v1
	v_sub_f32_e32 v1, v9, v180
	v_add_f32_e32 v33, v33, v21
	v_exp_f32_e32 v25, v25
	v_sub_f32_e32 v26, v26, v180
	v_add_f32_e32 v0, v0, v5
	v_exp_f32_e32 v9, v1
	v_sub_f32_e32 v1, v10, v180
	v_add_f32_e32 v33, v33, v22
	v_exp_f32_e32 v26, v26
	v_sub_f32_e32 v27, v27, v180
	v_add_f32_e32 v0, v0, v6
	v_exp_f32_e32 v10, v1
	v_sub_f32_e32 v1, v11, v180
	v_add_f32_e32 v33, v33, v23
	v_exp_f32_e32 v27, v27
	v_sub_f32_e32 v28, v28, v180
	v_add_f32_e32 v0, v0, v7
	v_exp_f32_e32 v11, v1
	v_sub_f32_e32 v1, v12, v180
	v_add_f32_e32 v33, v33, v24
	v_exp_f32_e32 v28, v28
	v_sub_f32_e32 v29, v29, v180
	v_add_f32_e32 v0, v0, v8
	v_exp_f32_e32 v12, v1
	v_sub_f32_e32 v1, v13, v180
	v_add_f32_e32 v33, v33, v25
	v_exp_f32_e32 v29, v29
	v_sub_f32_e32 v30, v30, v180
	v_add_f32_e32 v0, v0, v9
	v_exp_f32_e32 v13, v1
	v_sub_f32_e32 v1, v14, v180
	v_add_f32_e32 v33, v33, v26
	v_exp_f32_e32 v30, v30
	v_sub_f32_e32 v31, v31, v180
	v_add_f32_e32 v0, v0, v10
	v_exp_f32_e32 v14, v1
	v_sub_f32_e32 v1, v15, v180
	v_add_f32_e32 v33, v33, v27
	v_exp_f32_e32 v31, v31
	v_add_f32_e32 v0, v0, v11
	v_exp_f32_e32 v15, v1
	v_add_f32_e32 v33, v33, v28
	v_add_f32_e32 v0, v0, v12
	v_sub_f32_e32 v160, 0xf149f2ca, v180
	v_add_f32_e32 v33, v33, v29
	v_add_f32_e32 v0, v0, v13
	v_exp_f32_e32 v160, v160
	v_add_f32_e32 v33, v33, v30
	v_add_f32_e32 v0, v0, v14
	v_add_f32_e32 v33, v33, v31
	v_add_f32_e32 v0, v0, v15
	v_add_f32_e32 v0, v33, v0
	v_add_f32_e32 v212, v32, v0
	v_fmac_f32_e32 v212, 0, v160
	v_cvt_pk_f16_f32 v3, v54, v55
	v_cvt_pk_f16_f32 v2, v52, v53
	v_cvt_pk_f16_f32 v1, v50, v51
	v_cvt_pk_f16_f32 v0, v48, v49
	v_cvt_pk_f16_f32 v35, v62, v63
	v_cvt_pk_f16_f32 v34, v60, v61
	v_cvt_pk_f16_f32 v33, v58, v59
	v_cvt_pk_f16_f32 v32, v56, v57
	v_cvt_pk_f16_f32 v39, v38, v39
	v_cvt_pk_f16_f32 v38, v36, v37
	v_cvt_pk_f16_f32 v37, v164, v165
	v_cvt_pk_f16_f32 v36, v162, v163
	v_cvt_pk_f16_f32 v43, v43, v45
	v_cvt_pk_f16_f32 v42, v42, v44
	v_cvt_pk_f16_f32 v41, v41, v167
	v_cvt_pk_f16_f32 v40, v40, v166
	v_cvt_pk_f16_f32 v47, v22, v23
	v_cvt_pk_f16_f32 v46, v20, v21
	v_cvt_pk_f16_f32 v45, v18, v19
	v_cvt_pk_f16_f32 v44, v16, v17
	v_cvt_pk_f16_f32 v51, v30, v31
	v_cvt_pk_f16_f32 v50, v28, v29
	v_cvt_pk_f16_f32 v49, v26, v27
	v_cvt_pk_f16_f32 v48, v24, v25
	v_cvt_pk_f16_f32 v55, v6, v7
	v_cvt_pk_f16_f32 v54, v4, v5
	v_cvt_pk_f16_f32 v53, v169, v170
	v_cvt_pk_f16_f32 v52, v161, v168
	v_cvt_pk_f16_f32 v59, v14, v15
	v_cvt_pk_f16_f32 v58, v12, v13
	v_cvt_pk_f16_f32 v57, v10, v11
	v_cvt_pk_f16_f32 v56, v8, v9
	v_mfma_f32_32x32x16_f16 v[16:31], v[152:155], v[0:3], 0
	v_mfma_f32_32x32x16_f16 v[0:15], v[156:159], v[0:3], 0
	v_mfma_f32_32x32x16_f16 v[16:31], v[148:151], v[32:35], v[16:31]
	v_mfma_f32_32x32x16_f16 v[0:15], v[144:147], v[32:35], v[0:15]
	v_mfma_f32_32x32x16_f16 v[16:31], v[140:143], v[36:39], v[16:31]
	v_mfma_f32_32x32x16_f16 v[0:15], v[136:139], v[36:39], v[0:15]
	v_mfma_f32_32x32x16_f16 v[16:31], v[132:135], v[40:43], v[16:31]
	v_mfma_f32_32x32x16_f16 v[0:15], v[92:95], v[40:43], v[0:15]
	v_mfma_f32_32x32x16_f16 v[16:31], v[128:131], v[44:47], v[16:31]
	v_mfma_f32_32x32x16_f16 v[0:15], v[88:91], v[44:47], v[0:15]
	v_mfma_f32_32x32x16_f16 v[16:31], v[84:87], v[48:51], v[16:31]
	v_mfma_f32_32x32x16_f16 v[0:15], v[80:83], v[48:51], v[0:15]
	v_mfma_f32_32x32x16_f16 v[16:31], v[76:79], v[52:55], v[16:31]
	v_mfma_f32_32x32x16_f16 v[0:15], v[72:75], v[52:55], v[0:15]
	ds_read_b128 v[32:35], v186 offset:16384
	ds_read_b128 v[36:39], v186 offset:20480
	ds_read_b128 v[40:43], v187 offset:16384
	ds_read_b128 v[44:47], v187 offset:20480
	ds_read_b128 v[48:51], v188 offset:16384
	ds_read_b128 v[52:55], v188 offset:20480
	ds_read_b128 v[60:63], v189 offset:16384
	ds_read_b128 v[128:131], v189 offset:20480
	ds_read_b128 v[132:135], v186 offset:24576
	ds_read_b128 v[136:139], v186 offset:28672
	ds_read_b128 v[140:143], v187 offset:24576
	ds_read_b128 v[144:147], v187 offset:28672
	ds_read_b128 v[148:151], v188 offset:24576
	ds_read_b128 v[204:207], v188 offset:28672
	ds_read_b128 v[152:155], v189 offset:24576
	ds_read_b128 v[208:211], v189 offset:28672
	v_mfma_f32_32x32x16_f16 v[16:31], v[68:71], v[56:59], v[16:31]
	v_mfma_f32_32x32x16_f16 v[0:15], v[64:67], v[56:59], v[0:15]
	s_waitcnt lgkmcnt(14)
	v_mfma_f32_32x32x16_f16 v[80:95], v[32:35], v[120:123], 0
	s_waitcnt lgkmcnt(13)
	v_mfma_f32_32x32x16_f16 v[80:95], v[40:43], v[124:127], v[80:95]
	v_mfma_f32_32x32x16_f16 v[64:79], v[36:39], v[120:123], 0
	s_waitcnt lgkmcnt(11)
	v_mfma_f32_32x32x16_f16 v[80:95], v[48:51], v[116:119], v[80:95]
	v_mfma_f32_32x32x16_f16 v[64:79], v[44:47], v[124:127], v[64:79]
	s_waitcnt lgkmcnt(9)
	v_mfma_f32_32x32x16_f16 v[80:95], v[60:63], v[112:115], v[80:95]
	v_mfma_f32_32x32x16_f16 v[64:79], v[52:55], v[116:119], v[64:79]
	s_waitcnt lgkmcnt(7)
	v_mfma_f32_32x32x16_f16 v[48:63], v[132:135], v[120:123], 0
	s_waitcnt lgkmcnt(5)
	v_mfma_f32_32x32x16_f16 v[48:63], v[140:143], v[124:127], v[48:63]
	v_mfma_f32_32x32x16_f16 v[32:47], v[136:139], v[120:123], 0
	s_waitcnt lgkmcnt(3)
	v_mfma_f32_32x32x16_f16 v[48:63], v[148:151], v[116:119], v[48:63]
	v_mfma_f32_32x32x16_f16 v[32:47], v[144:147], v[124:127], v[32:47]
	v_mfma_f32_32x32x16_f16 v[64:79], v[128:131], v[112:115], v[64:79]
	s_waitcnt lgkmcnt(1)
	v_mfma_f32_32x32x16_f16 v[48:63], v[152:155], v[112:115], v[48:63]
	ds_read_b128 v[176:179], v190 offset:33024
	ds_read_b128 v[172:175], v190 offset:49408
	ds_read_b128 v[168:171], v191 offset:33024
	ds_read_b128 v[164:167], v191 offset:49408
	ds_read_b128 v[160:163], v192 offset:33024
	ds_read_b128 v[156:159], v192 offset:49408
	ds_read_b128 v[152:155], v193 offset:33024
	ds_read_b128 v[132:135], v193 offset:49408
	v_mfma_f32_32x32x16_f16 v[32:47], v[204:207], v[116:119], v[32:47]
	ds_read_b128 v[148:151], v194 offset:33024
	ds_read_b128 v[128:131], v194 offset:49408
	ds_read_b128 v[144:147], v195 offset:33024
	ds_read_b128 v[124:127], v195 offset:49408
	ds_read_b128 v[140:143], v196 offset:33024
	ds_read_b128 v[120:123], v196 offset:49408
	ds_read_b128 v[136:139], v197 offset:33024
	ds_read_b128 v[116:119], v197 offset:49408
	s_waitcnt lgkmcnt(14)
	v_mfma_f32_32x32x16_f16 v[32:47], v[208:211], v[112:115], v[32:47]
	v_max_f32_e32 v112, v81, v81
	v_max_f32_e32 v113, v80, v80
	s_nop 9
	v_max_f32_e32 v115, v33, v33
	v_max_f32_e32 v204, v32, v32
	v_max_f32_e32 v112, v113, v112
	v_max_f32_e32 v113, v65, v65
	v_max_f32_e32 v114, v64, v64
	v_max_f32_e32 v115, v204, v115
	v_max_f32_e32 v113, v114, v113
	v_max3_f32 v114, v48, v49, v50
	v_max3_f32 v115, v115, v34, v35
	v_max3_f32 v112, v112, v82, v83
	v_max3_f32 v113, v113, v66, v67
	v_max3_f32 v114, v114, v51, v52
	v_max3_f32 v115, v115, v36, v37
	v_max3_f32 v112, v112, v84, v85
	v_max3_f32 v113, v113, v68, v69
	v_max3_f32 v114, v114, v53, v54
	v_max3_f32 v115, v115, v38, v39
	v_max3_f32 v112, v112, v86, v87
	v_max3_f32 v113, v113, v70, v71
	v_max3_f32 v114, v114, v55, v56
	v_max3_f32 v115, v115, v40, v41
	v_max3_f32 v112, v112, v88, v89
	v_max3_f32 v113, v113, v72, v73
	v_max3_f32 v114, v114, v57, v58
	v_max3_f32 v115, v115, v42, v43
	v_max3_f32 v112, v112, v90, v91
	v_max3_f32 v113, v113, v74, v75
	v_max3_f32 v114, v114, v59, v60
	v_max3_f32 v115, v115, v44, v45
	v_max3_f32 v112, v112, v92, v93
	v_max3_f32 v113, v113, v76, v77
	v_max3_f32 v114, v114, v61, v62
	v_max3_f32 v115, v115, v46, v47
	v_max3_f32 v112, v112, v94, v95
	v_max3_f32 v113, v113, v78, v79
	v_max3_f32 v114, v114, v63, v115
	v_max3_f32 v112, v112, v113, v114
	ds_bpermute_b32 v113, v198, v112
	s_waitcnt lgkmcnt(0)
	v_max3_f32 v113, v180, v112, v113
	v_sub_f32_e32 v49, v49, v113
	v_exp_f32_e32 v205, v49
	v_sub_f32_e32 v49, v50, v113
	v_sub_f32_e32 v50, v51, v113
	v_sub_f32_e32 v51, v52, v113
	v_exp_f32_e32 v52, v51
	v_sub_f32_e32 v51, v53, v113
	v_exp_f32_e32 v53, v51
	v_sub_f32_e32 v51, v54, v113
	v_sub_f32_e32 v54, v55, v113
	v_sub_f32_e32 v55, v56, v113
	v_exp_f32_e32 v56, v55
	v_sub_f32_e32 v55, v57, v113
	v_exp_f32_e32 v57, v55
	v_sub_f32_e32 v55, v58, v113
	v_exp_f32_e32 v58, v55
	v_sub_f32_e32 v55, v59, v113
	v_exp_f32_e32 v59, v55
	v_sub_f32_e32 v55, v60, v113
	v_sub_f32_e32 v80, v80, v113
	v_sub_f32_e32 v64, v64, v113
	v_sub_f32_e32 v48, v48, v113
	v_exp_f32_e32 v60, v55
	v_sub_f32_e32 v55, v61, v113
	v_sub_f32_e32 v32, v32, v113
	v_sub_f32_e32 v112, v180, v113
	v_exp_f32_e32 v114, v80
	v_sub_f32_e32 v80, v81, v113
	v_exp_f32_e32 v180, v64
	v_sub_f32_e32 v64, v65, v113
	v_exp_f32_e32 v48, v48
	v_exp_f32_e32 v61, v55
	v_sub_f32_e32 v55, v62, v113
	v_sub_f32_e32 v62, v63, v113
	v_exp_f32_e32 v63, v32
	v_sub_f32_e32 v32, v33, v113
	v_exp_f32_e32 v115, v80
	v_sub_f32_e32 v80, v82, v113
	v_exp_f32_e32 v204, v64
	v_sub_f32_e32 v64, v66, v113
	v_exp_f32_e32 v207, v32
	v_sub_f32_e32 v32, v34, v113
	v_exp_f32_e32 v82, v80
	v_sub_f32_e32 v80, v83, v113
	v_exp_f32_e32 v66, v64
	v_sub_f32_e32 v64, v67, v113
	v_exp_f32_e32 v49, v49
	v_exp_f32_e32 v208, v32
	v_sub_f32_e32 v32, v35, v113
	v_exp_f32_e32 v83, v80
	v_sub_f32_e32 v81, v84, v113
	v_exp_f32_e32 v67, v64
	v_sub_f32_e32 v65, v68, v113
	v_exp_f32_e32 v206, v50
	v_exp_f32_e32 v209, v32
	v_sub_f32_e32 v33, v36, v113
	v_add_f32_e32 v80, 0, v114
	v_exp_f32_e32 v84, v81
	v_sub_f32_e32 v81, v85, v113
	v_add_f32_e32 v64, 0, v180
	v_exp_f32_e32 v68, v65
	v_sub_f32_e32 v65, v69, v113
	v_add_f32_e32 v50, 0, v48
	v_add_f32_e32 v32, 0, v63
	v_exp_f32_e32 v210, v33
	v_sub_f32_e32 v33, v37, v113
	v_add_f32_e32 v80, v80, v115
	v_exp_f32_e32 v85, v81
	v_sub_f32_e32 v81, v86, v113
	v_add_f32_e32 v64, v64, v204
	v_exp_f32_e32 v69, v65
	v_sub_f32_e32 v65, v70, v113
	v_add_f32_e32 v50, v50, v205
	v_add_f32_e32 v32, v32, v207
	v_exp_f32_e32 v211, v33
	v_sub_f32_e32 v33, v38, v113
	v_add_f32_e32 v80, v80, v82
	v_exp_f32_e32 v86, v81
	v_sub_f32_e32 v81, v87, v113
	v_add_f32_e32 v64, v64, v66
	v_exp_f32_e32 v70, v65
	v_sub_f32_e32 v65, v71, v113
	v_add_f32_e32 v50, v50, v49
	v_exp_f32_e32 v51, v51
	v_add_f32_e32 v32, v32, v208
	v_exp_f32_e32 v213, v33
	v_sub_f32_e32 v33, v39, v113
	v_add_f32_e32 v80, v80, v83
	v_exp_f32_e32 v87, v81
	v_sub_f32_e32 v81, v88, v113
	v_add_f32_e32 v64, v64, v67
	v_exp_f32_e32 v71, v65
	v_sub_f32_e32 v65, v72, v113
	v_add_f32_e32 v50, v50, v206
	v_exp_f32_e32 v54, v54
	v_add_f32_e32 v32, v32, v209
	v_exp_f32_e32 v214, v33
	v_sub_f32_e32 v33, v40, v113
	v_add_f32_e32 v80, v80, v84
	v_exp_f32_e32 v88, v81
	v_sub_f32_e32 v81, v89, v113
	v_add_f32_e32 v64, v64, v68
	v_exp_f32_e32 v72, v65
	v_sub_f32_e32 v65, v73, v113
	v_add_f32_e32 v50, v50, v52
	v_add_f32_e32 v32, v32, v210
	v_exp_f32_e32 v215, v33
	v_sub_f32_e32 v33, v41, v113
	v_add_f32_e32 v80, v80, v85
	v_exp_f32_e32 v89, v81
	v_sub_f32_e32 v81, v90, v113
	v_add_f32_e32 v64, v64, v69
	v_exp_f32_e32 v73, v65
	v_sub_f32_e32 v65, v74, v113
	v_add_f32_e32 v50, v50, v53
	v_add_f32_e32 v32, v32, v211
	v_exp_f32_e32 v216, v33
	v_sub_f32_e32 v33, v42, v113
	v_add_f32_e32 v80, v80, v86
	v_exp_f32_e32 v90, v81
	v_sub_f32_e32 v81, v91, v113
	v_add_f32_e32 v64, v64, v70
	v_exp_f32_e32 v74, v65
	v_sub_f32_e32 v65, v75, v113
	v_add_f32_e32 v50, v50, v51
	v_add_f32_e32 v32, v32, v213
	v_exp_f32_e32 v217, v33
	v_sub_f32_e32 v33, v43, v113
	v_add_f32_e32 v80, v80, v87
	v_exp_f32_e32 v91, v81
	v_sub_f32_e32 v81, v92, v113
	v_add_f32_e32 v64, v64, v71
	v_exp_f32_e32 v75, v65
	v_sub_f32_e32 v65, v76, v113
	v_add_f32_e32 v50, v50, v54
	v_add_f32_e32 v32, v32, v214
	v_exp_f32_e32 v218, v33
	v_sub_f32_e32 v33, v44, v113
	v_add_f32_e32 v80, v80, v88
	v_exp_f32_e32 v92, v81
	v_sub_f32_e32 v81, v93, v113
	v_add_f32_e32 v64, v64, v72
	v_exp_f32_e32 v76, v65
	v_sub_f32_e32 v65, v77, v113
	v_add_f32_e32 v50, v50, v56
	v_add_f32_e32 v32, v32, v215
	v_exp_f32_e32 v219, v33
	v_sub_f32_e32 v33, v45, v113
	v_add_f32_e32 v80, v80, v89
	v_exp_f32_e32 v93, v81
	v_sub_f32_e32 v81, v94, v113
	v_add_f32_e32 v64, v64, v73
	v_exp_f32_e32 v77, v65
	v_sub_f32_e32 v65, v78, v113
	v_add_f32_e32 v50, v50, v57
	v_add_f32_e32 v32, v32, v216
	v_exp_f32_e32 v220, v33
	v_sub_f32_e32 v33, v46, v113
	v_add_f32_e32 v80, v80, v90
	v_exp_f32_e32 v94, v81
	v_sub_f32_e32 v81, v95, v113
	v_add_f32_e32 v64, v64, v74
	v_exp_f32_e32 v78, v65
	v_sub_f32_e32 v65, v79, v113
	v_add_f32_e32 v50, v50, v58
	v_exp_f32_e32 v55, v55
	v_add_f32_e32 v32, v32, v217
	v_exp_f32_e32 v221, v33
	v_sub_f32_e32 v33, v47, v113
	v_add_f32_e32 v80, v80, v91
	v_exp_f32_e32 v95, v81
	v_add_f32_e32 v64, v64, v75
	v_exp_f32_e32 v79, v65
	v_add_f32_e32 v50, v50, v59
	v_exp_f32_e32 v62, v62
	v_add_f32_e32 v32, v32, v218
	v_exp_f32_e32 v113, v33
	v_add_f32_e32 v80, v80, v92
	v_add_f32_e32 v64, v64, v76
	v_add_f32_e32 v50, v50, v60
	v_add_f32_e32 v32, v32, v219
	v_add_f32_e32 v80, v80, v93
	v_add_f32_e32 v64, v64, v77
	v_add_f32_e32 v50, v50, v61
	v_add_f32_e32 v32, v32, v220
	v_exp_f32_e32 v112, v112
	v_add_f32_e32 v80, v80, v94
	v_add_f32_e32 v64, v64, v78
	v_add_f32_e32 v50, v50, v55
	v_add_f32_e32 v32, v32, v221
	v_add_f32_e32 v80, v80, v95
	v_add_f32_e32 v64, v64, v79
	v_add_f32_e32 v81, v50, v62
	v_add_f32_e32 v65, v32, v113
	v_pk_add_f32 v[32:33], v[80:81], v[64:65]
	v_cvt_pk_f16_f32 v35, v86, v87
	v_add_f32_e32 v64, v32, v33
	v_fmac_f32_e32 v64, v212, v112
	v_cvt_pk_f16_f32 v34, v84, v85
	v_cvt_pk_f16_f32 v33, v82, v83
	v_cvt_pk_f16_f32 v32, v114, v115
	v_cvt_pk_f16_f32 v39, v94, v95
	v_cvt_pk_f16_f32 v38, v92, v93
	v_cvt_pk_f16_f32 v37, v90, v91
	v_cvt_pk_f16_f32 v36, v88, v89
	v_cvt_pk_f16_f32 v43, v70, v71
	v_cvt_pk_f16_f32 v42, v68, v69
	v_cvt_pk_f16_f32 v41, v66, v67
	v_cvt_pk_f16_f32 v40, v180, v204
	v_cvt_pk_f16_f32 v47, v78, v79
	v_cvt_pk_f16_f32 v46, v76, v77
	v_cvt_pk_f16_f32 v45, v74, v75
	v_cvt_pk_f16_f32 v44, v72, v73
	v_cvt_pk_f16_f32 v51, v51, v54
	v_cvt_pk_f16_f32 v50, v52, v53
	v_cvt_pk_f16_f32 v49, v49, v206
	v_cvt_pk_f16_f32 v48, v48, v205
	v_cvt_pk_f16_f32 v55, v55, v62
	v_cvt_pk_f16_f32 v54, v60, v61
	v_cvt_pk_f16_f32 v53, v58, v59
	v_cvt_pk_f16_f32 v52, v56, v57
	v_cvt_pk_f16_f32 v59, v213, v214
	v_cvt_pk_f16_f32 v58, v210, v211
	v_cvt_pk_f16_f32 v57, v208, v209
	v_cvt_pk_f16_f32 v56, v63, v207
	v_cvt_pk_f16_f32 v63, v221, v113
	v_cvt_pk_f16_f32 v62, v219, v220
	v_cvt_pk_f16_f32 v61, v217, v218
	v_cvt_pk_f16_f32 v60, v215, v216
	v_pk_mul_f32 v[30:31], v[112:113], v[30:31] op_sel_hi:[0,1]
	v_pk_mul_f32 v[28:29], v[112:113], v[28:29] op_sel_hi:[0,1]
	v_pk_mul_f32 v[26:27], v[112:113], v[26:27] op_sel_hi:[0,1]
	v_pk_mul_f32 v[24:25], v[112:113], v[24:25] op_sel_hi:[0,1]
	v_pk_mul_f32 v[22:23], v[112:113], v[22:23] op_sel_hi:[0,1]
	v_pk_mul_f32 v[20:21], v[112:113], v[20:21] op_sel_hi:[0,1]
	v_pk_mul_f32 v[18:19], v[112:113], v[18:19] op_sel_hi:[0,1]
	v_pk_mul_f32 v[16:17], v[112:113], v[16:17] op_sel_hi:[0,1]
	v_pk_mul_f32 v[14:15], v[112:113], v[14:15] op_sel_hi:[0,1]
	v_pk_mul_f32 v[12:13], v[112:113], v[12:13] op_sel_hi:[0,1]
	v_mfma_f32_32x32x16_f16 v[16:31], v[176:179], v[32:35], v[16:31]
	v_mul_f32_e64 v10, v112, v10
	v_mul_f32_e64 v11, v112, v11
	v_mul_f32_e64 v8, v112, v8
	v_mul_f32_e64 v9, v112, v9
	v_mul_f32_e64 v6, v112, v6
	v_mul_f32_e64 v7, v112, v7
	v_pk_mul_f32 v[4:5], v[112:113], v[4:5] op_sel_hi:[0,1]
	v_pk_mul_f32 v[2:3], v[112:113], v[2:3] op_sel_hi:[0,1]
	v_pk_mul_f32 v[0:1], v[112:113], v[0:1] op_sel_hi:[0,1]
	v_add_u32_e32 v180, s1, v200
	v_mfma_f32_32x32x16_f16 v[16:31], v[168:171], v[36:39], v[16:31]
	s_addk_i32 s1, 0x100
	s_waitcnt vmcnt(0)
	v_mov_b64_e32 v[114:115], v[110:111]
	s_cmpk_eq_i32 s1, 0x400
	s_cselect_b32 s1, 0x380, s1
	s_cmp_eq_u32 s1, s15
	v_mov_b64_e32 v[112:113], v[108:109]
	v_mfma_f32_32x32x16_f16 v[16:31], v[160:163], v[40:43], v[16:31]
	v_mfma_f32_32x32x16_f16 v[0:15], v[172:175], v[32:35], v[0:15]
	ds_bpermute_b32 v32, v198, v64
	s_waitcnt lgkmcnt(0)
	v_add_f32_e32 v32, v64, v32
	v_div_scale_f32 v33, s[2:3], v32, v32, 1.0
	v_mfma_f32_32x32x16_f16 v[16:31], v[152:155], v[44:47], v[16:31]
	v_rcp_f32_e32 v34, v33
	s_nop 0
	v_fma_f32 v35, -v33, v34, 1.0
	v_fmac_f32_e32 v34, v35, v34
	v_div_scale_f32 v35, vcc, 1.0, v32, 1.0
	v_mfma_f32_32x32x16_f16 v[0:15], v[164:167], v[36:39], v[0:15]
	v_mul_f32_e32 v36, v35, v34
	v_fma_f32 v37, -v33, v36, v35
	v_fmac_f32_e32 v36, v37, v34
	v_fma_f32 v33, -v33, v36, v35
	v_div_fmas_f32 v33, v33, v34, v36
	v_div_fixup_f32 v32, v33, v32, 1.0
	v_mfma_f32_32x32x16_f16 v[16:31], v[148:151], v[48:51], v[16:31]
	v_mfma_f32_32x32x16_f16 v[0:15], v[156:159], v[40:43], v[0:15]
	v_mfma_f32_32x32x16_f16 v[16:31], v[144:147], v[52:55], v[16:31]
	v_mfma_f32_32x32x16_f16 v[0:15], v[132:135], v[44:47], v[0:15]
	v_mfma_f32_32x32x16_f16 v[16:31], v[140:143], v[56:59], v[16:31]
	v_mfma_f32_32x32x16_f16 v[0:15], v[128:131], v[48:51], v[0:15]
	v_mfma_f32_32x32x16_f16 v[16:31], v[136:139], v[60:63], v[16:31]
	v_mfma_f32_32x32x16_f16 v[0:15], v[124:127], v[52:55], v[0:15]
	s_nop 10
	v_fma_mixlo_f16 v33, v32, v16, 0
	v_mov_b32_e32 v16, v17
	v_mov_b32_e32 v17, v18
	v_mul_f32_e64 v16, v32, v16
	v_mul_f32_e64 v17, v32, v17
	v_cvt_pk_f16_f32 v17, v16, v17
	v_fma_mixlo_f16 v18, v32, v19, 0
	v_pack_b32_f16 v16, v33, v17
	v_mfma_f32_32x32x16_f16 v[0:15], v[120:123], v[56:59], v[0:15]
	v_alignbit_b32 v17, v18, v17, 16
	v_mov_b32_e32 v18, v21
	v_mov_b32_e32 v19, v22
	v_mul_f32_e64 v18, v32, v18
	v_mul_f32_e64 v19, v32, v19
	v_fma_mixlo_f16 v20, v32, v20, 0
	v_cvt_pk_f16_f32 v19, v18, v19
	v_pack_b32_f16 v18, v20, v19
	v_fma_mixlo_f16 v20, v32, v23, 0
	v_alignbit_b32 v19, v20, v19, 16
	ds_write2_b64 v201, v[16:17], v[18:19] offset1:2
	v_mov_b32_e32 v16, v25
	v_mov_b32_e32 v17, v26
	v_pk_mul_f32 v[16:17], v[32:33], v[16:17] op_sel_hi:[0,1]
	v_mfma_f32_32x32x16_f16 v[0:15], v[116:119], v[60:63], v[0:15]
	v_fma_mixlo_f16 v18, v32, v24, 0
	v_cvt_pk_f16_f32 v17, v16, v17
	v_pack_b32_f16 v16, v18, v17
	v_fma_mixlo_f16 v18, v32, v27, 0
	v_alignbit_b32 v17, v18, v17, 16
	v_mov_b32_e32 v18, v29
	v_mov_b32_e32 v19, v30
	v_pk_mul_f32 v[18:19], v[32:33], v[18:19] op_sel_hi:[0,1]
	v_fma_mixlo_f16 v20, v32, v28, 0
	v_cvt_pk_f16_f32 v19, v18, v19
	v_pack_b32_f16 v18, v20, v19
	v_fma_mixlo_f16 v20, v32, v31, 0
	v_alignbit_b32 v19, v20, v19, 16
	ds_write2_b64 v201, v[16:17], v[18:19] offset0:4 offset1:6
	v_fma_mixlo_f16 v16, v32, v0, 0
	v_mov_b32_e32 v0, v1
	v_mov_b32_e32 v1, v2
	v_pk_mul_f32 v[0:1], v[32:33], v[0:1] op_sel_hi:[0,1]
	v_cvt_pk_f16_f32 v1, v0, v1
	v_fma_mixlo_f16 v2, v32, v3, 0
	v_pack_b32_f16 v0, v16, v1
	v_alignbit_b32 v1, v2, v1, 16
	v_mov_b32_e32 v2, v5
	v_mov_b32_e32 v3, v6
	v_pk_mul_f32 v[2:3], v[32:33], v[2:3] op_sel_hi:[0,1]
	v_fma_mixlo_f16 v4, v32, v4, 0
	v_cvt_pk_f16_f32 v3, v2, v3
	v_pack_b32_f16 v2, v4, v3
	v_fma_mixlo_f16 v4, v32, v7, 0
	v_alignbit_b32 v3, v4, v3, 16
	ds_write2_b64 v201, v[0:1], v[2:3] offset0:8 offset1:10
	v_mov_b32_e32 v0, v9
	v_mov_b32_e32 v1, v10
	v_pk_mul_f32 v[0:1], v[32:33], v[0:1] op_sel_hi:[0,1]
	v_fma_mixlo_f16 v2, v32, v8, 0
	v_cvt_pk_f16_f32 v1, v0, v1
	v_pack_b32_f16 v0, v2, v1
	v_fma_mixlo_f16 v2, v32, v11, 0
	v_alignbit_b32 v1, v2, v1, 16
	v_mov_b32_e32 v2, v13
	v_mov_b32_e32 v3, v14
	v_pk_mul_f32 v[2:3], v[32:33], v[2:3] op_sel_hi:[0,1]
	v_fma_mixlo_f16 v4, v32, v12, 0
	v_cvt_pk_f16_f32 v3, v2, v3
	v_pack_b32_f16 v2, v4, v3
	v_fma_mixlo_f16 v4, v32, v15, 0
	v_alignbit_b32 v3, v4, v3, 16
	ds_write2_b64 v201, v[0:1], v[2:3] offset0:12 offset1:14
	s_waitcnt lgkmcnt(0)
	ds_read_b128 v[0:3], v202
	v_lshlrev_b64 v[4:5], 11, v[180:181]
	v_lshl_add_u64 v[8:9], v[184:185], 0, v[4:5]
	ds_read_b128 v[4:7], v203
	v_mov_b64_e32 v[122:123], v[98:99]
	s_waitcnt lgkmcnt(1)
	global_store_dwordx4 v[8:9], v[0:3], off sc0 sc1
	v_mov_b64_e32 v[126:127], v[102:103]
	v_mov_b64_e32 v[118:119], v[106:107]
	v_add_u32_e32 v0, 8, v180
	v_mov_b32_e32 v1, v181
	v_lshlrev_b64 v[0:1], 11, v[0:1]
	v_lshl_add_u64 v[0:1], v[184:185], 0, v[0:1]
	s_waitcnt lgkmcnt(0)
	global_store_dwordx4 v[0:1], v[4:7], off sc0 sc1
	ds_read_b128 v[0:3], v203 offset:1152
	v_mov_b64_e32 v[120:121], v[96:97]
	v_add_u32_e32 v4, 16, v180
	v_mov_b32_e32 v5, v181
	v_lshlrev_b64 v[4:5], 11, v[4:5]
	v_lshl_add_u64 v[8:9], v[184:185], 0, v[4:5]
	ds_read_b128 v[4:7], v203 offset:2304
	v_add_u32_e32 v180, 24, v180
	s_waitcnt lgkmcnt(1)
	global_store_dwordx4 v[8:9], v[0:3], off sc0 sc1
	v_mov_b64_e32 v[124:125], v[100:101]
	v_mov_b64_e32 v[116:117], v[104:105]
	v_lshlrev_b64 v[0:1], 11, v[180:181]
	v_lshl_add_u64 v[0:1], v[184:185], 0, v[0:1]
	s_waitcnt lgkmcnt(0)
	global_store_dwordx4 v[0:1], v[4:7], off sc0 sc1
	s_waitcnt lgkmcnt(0)
	s_cbranch_scc1 .LBB5_4
.LBB5_2:
	s_cmp_eq_u32 s1, s14
	s_cbranch_scc1 .LBB5_1
	s_cmpk_eq_i32 s1, 0x300
	s_cselect_b32 s17, 0x280, s1
	v_add_u32_e32 v180, s17, v199
	v_lshlrev_b64 v[0:1], 11, v[180:181]
	v_lshl_add_u64 v[0:1], v[182:183], 0, v[0:1]
	global_load_dwordx4 v[96:99], v[0:1], off
	global_load_dwordx4 v[100:103], v[0:1], off offset:32
	global_load_dwordx4 v[104:107], v[0:1], off offset:64
	global_load_dwordx4 v[108:111], v[0:1], off offset:96
	s_branch .LBB5_1
